# baseline (speedup 1.0000x reference)
.LBB1_8:
	s_or_b64 exec, exec, s[4:5]
	s_waitcnt vmcnt(1)
	v_mov_b32_e32 v184, 1
	v_lshl_add_u32 v180, v176, 2, v172
	v_lshl_add_u32 v181, v177, 2, v172
	v_lshl_add_u32 v182, v178, 2, v172
	v_lshl_add_u32 v183, v179, 2, v172
	s_waitcnt lgkmcnt(0)
	ds_add_u32 v180, v184
	ds_add_u32 v181, v184
	ds_add_u32 v182, v184
	ds_add_u32 v183, v184
	s_waitcnt lgkmcnt(0)
	ds_read_b32 v151, v173
	s_waitcnt lgkmcnt(0)
	v_cvt_f32_i32_e32 v185, v151
	ds_write_b32 v173, v185 offset:256
	v_add_u32_e32 v10, v172, v2
	s_waitcnt vmcnt(1) lgkmcnt(0)
	s_barrier
	s_nop 0
	s_nop 0
	ds_read_b128 v[18:21], v10 offset:256
	ds_read_b128 v[22:25], v10 offset:288
	ds_read_b128 v[82:85], v10 offset:320
	ds_read_b128 v[86:89], v10 offset:352
	ds_read_b128 v[74:77], v10 offset:384
	ds_read_b128 v[78:81], v10 offset:416
	ds_read_b128 v[2:5], v213 offset:32768
	ds_read_b128 v[6:9], v213 offset:0
	ds_read_b128 v[66:69], v10 offset:448
	ds_read_b128 v[70:73], v10 offset:480
	ds_read_b128 v[10:13], v213 offset:1024
	s_waitcnt lgkmcnt(3)
	v_pk_mul_f32 v[26:27], v[8:9], v[20:21]
	v_pk_mul_f32 v[28:29], v[6:7], v[18:19]
	ds_read_b128 v[14:17], v213 offset:8192
	s_waitcnt lgkmcnt(1)
	v_pk_mul_f32 v[12:13], v[12:13], v[24:25]
	v_pk_mul_f32 v[10:11], v[10:11], v[22:23]
	v_pk_fma_f32 v[30:31], v[8:9], v[20:21], v[12:13]
	v_pk_fma_f32 v[32:33], v[6:7], v[18:19], v[10:11]
	v_cvt_pk_bf16_f32 v9, v12, v13
	v_cvt_pk_bf16_f32 v7, v26, v27
	v_cvt_pk_bf16_f32 v8, v10, v11
	v_cvt_pk_bf16_f32 v6, v28, v29
	ds_read_b128 v[10:13], v213 offset:33792
	s_nop 0
	v_mfma_f32_32x32x16_bf16 v[34:49], v[2:5], v[6:9], 0
	ds_read_b128 v[6:9], v213 offset:9216
	s_waitcnt lgkmcnt(2)
	v_mul_f32_e32 v26, v16, v20
	v_mul_f32_e32 v27, v17, v21
	v_pk_mul_f32 v[50:51], v[14:15], v[18:19]
	s_mov_b32 s4, 0x3727c5ac
	s_waitcnt lgkmcnt(0)
	v_pk_mul_f32 v[8:9], v[8:9], v[24:25]
	v_pk_mul_f32 v[28:29], v[6:7], v[22:23]
	v_pk_fma_f32 v[90:91], v[16:17], v[20:21], v[8:9]
	v_pk_fma_f32 v[92:93], v[14:15], v[18:19], v[28:29]
	ds_read_b128 v[14:17], v213 offset:2048
	v_cvt_pk_bf16_f32 v9, v8, v9
	v_cvt_pk_bf16_f32 v7, v26, v27
	v_cvt_pk_bf16_f32 v8, v28, v29
	ds_read_b128 v[26:29], v213 offset:3072
	v_cvt_pk_bf16_f32 v6, v50, v51
	s_waitcnt lgkmcnt(1)
	v_pk_mul_f32 v[94:95], v[14:15], v[82:83]
	s_mov_b32 s0, 0x3c800000
	v_mfma_f32_32x32x16_bf16 v[50:65], v[2:5], v[6:9], 0
	v_mul_f32_e32 v2, v16, v84
	v_mul_f32_e32 v3, v17, v85
	s_waitcnt lgkmcnt(0)
	v_mul_f32_e32 v4, v28, v88
	v_mul_f32_e32 v5, v29, v89
	v_pk_mul_f32 v[6:7], v[26:27], v[86:87]
	v_pk_fma_f32 v[8:9], v[16:17], v[84:85], v[4:5]
	v_cvt_pk_bf16_f32 v3, v2, v3
	v_pk_fma_f32 v[14:15], v[14:15], v[82:83], v[6:7]
	v_pk_add_f32 v[26:27], v[8:9], v[30:31]
	v_cvt_pk_bf16_f32 v5, v4, v5
	v_cvt_pk_bf16_f32 v4, v6, v7
	ds_read_b128 v[6:9], v213 offset:10240
	v_pk_add_f32 v[28:29], v[14:15], v[32:33]
	ds_read_b128 v[14:17], v213 offset:11264
	v_cvt_pk_bf16_f32 v2, v94, v95
	s_waitcnt lgkmcnt(1)
	v_pk_mul_f32 v[30:31], v[6:7], v[82:83]
	v_mov_b64_e32 v[152:153], s[4:5]
	v_mfma_f32_32x32x16_bf16 v[34:49], v[10:13], v[2:5], v[34:49]
	v_mul_f32_e32 v2, v8, v84
	v_mul_f32_e32 v3, v9, v85
	s_waitcnt lgkmcnt(0)
	v_mul_f32_e32 v4, v16, v88
	v_mul_f32_e32 v5, v17, v89
	v_pk_mul_f32 v[14:15], v[14:15], v[86:87]
	v_pk_fma_f32 v[8:9], v[8:9], v[84:85], v[4:5]
	v_pk_fma_f32 v[6:7], v[6:7], v[82:83], v[14:15]
	v_cvt_pk_bf16_f32 v5, v4, v5
	v_cvt_pk_bf16_f32 v3, v2, v3
	v_cvt_pk_bf16_f32 v4, v14, v15
	v_pk_add_f32 v[32:33], v[8:9], v[90:91]
	v_pk_add_f32 v[90:91], v[6:7], v[92:93]
	ds_read_b128 v[6:9], v213 offset:34816
	ds_read_b128 v[14:17], v213 offset:4096
	v_cvt_pk_bf16_f32 v2, v30, v31
	s_mov_b32 s13, 0
	s_mov_b64 s[6:7], 0
	v_mfma_f32_32x32x16_bf16 v[50:65], v[10:13], v[2:5], v[50:65]
	ds_read_b128 v[2:5], v213 offset:5120
	ds_read_b128 v[10:13], v213 offset:12288
	s_waitcnt lgkmcnt(2)
	v_pk_mul_f32 v[30:31], v[16:17], v[76:77]
	v_pk_mul_f32 v[92:93], v[14:15], v[74:75]
	s_waitcnt lgkmcnt(1)
	v_pk_mul_f32 v[4:5], v[4:5], v[80:81]
	v_pk_mul_f32 v[94:95], v[2:3], v[78:79]
	v_pk_fma_f32 v[2:3], v[16:17], v[76:77], v[4:5]
	v_cvt_pk_bf16_f32 v5, v4, v5
	v_pk_add_f32 v[96:97], v[2:3], v[26:27]
	v_cvt_pk_bf16_f32 v3, v30, v31
	v_cvt_pk_bf16_f32 v4, v94, v95
	v_cvt_pk_bf16_f32 v2, v92, v93
	v_pk_fma_f32 v[14:15], v[14:15], v[74:75], v[94:95]
	s_waitcnt lgkmcnt(0)
	v_pk_mul_f32 v[30:31], v[10:11], v[74:75]
	v_mfma_f32_32x32x16_bf16 v[34:49], v[6:9], v[2:5], v[34:49]
	ds_read_b128 v[2:5], v213 offset:13312
	v_add_f32_e32 v98, v14, v28
	v_add_f32_e32 v99, v15, v29
	ds_read_b128 v[14:17], v213 offset:35840
	v_pk_mul_f32 v[26:27], v[12:13], v[76:77]
	s_waitcnt lgkmcnt(1)
	v_pk_mul_f32 v[4:5], v[4:5], v[80:81]
	v_pk_mul_f32 v[28:29], v[2:3], v[78:79]
	v_pk_fma_f32 v[2:3], v[12:13], v[76:77], v[4:5]
	v_pk_fma_f32 v[10:11], v[10:11], v[74:75], v[28:29]
	v_pk_add_f32 v[32:33], v[2:3], v[32:33]
	v_pk_add_f32 v[92:93], v[10:11], v[90:91]
	ds_read_b128 v[10:13], v213 offset:6144
	v_cvt_pk_bf16_f32 v5, v4, v5
	v_cvt_pk_bf16_f32 v3, v26, v27
	v_cvt_pk_bf16_f32 v4, v28, v29
	ds_read_b128 v[26:29], v213 offset:7168
	v_cvt_pk_bf16_f32 v2, v30, v31
	s_waitcnt lgkmcnt(1)
	v_pk_mul_f32 v[30:31], v[10:11], v[66:67]
	v_mfma_f32_32x32x16_bf16 v[50:65], v[6:9], v[2:5], v[50:65]
	v_mul_f32_e32 v2, v12, v68
	v_mul_f32_e32 v3, v13, v69
	s_waitcnt lgkmcnt(0)
	v_mul_f32_e32 v4, v28, v72
	v_mul_f32_e32 v5, v29, v73
	v_pk_mul_f32 v[6:7], v[26:27], v[70:71]
	v_pk_fma_f32 v[8:9], v[12:13], v[68:69], v[4:5]
	v_cvt_pk_bf16_f32 v3, v2, v3
	v_pk_fma_f32 v[10:11], v[10:11], v[66:67], v[6:7]
	v_pk_add_f32 v[94:95], v[8:9], v[96:97]
	v_cvt_pk_bf16_f32 v5, v4, v5
	v_cvt_pk_bf16_f32 v4, v6, v7
	ds_read_b128 v[6:9], v213 offset:14336
	v_pk_add_f32 v[96:97], v[10:11], v[98:99]
	ds_read_b128 v[10:13], v213 offset:15360
	v_cvt_pk_bf16_f32 v2, v30, v31
	s_waitcnt lgkmcnt(1)
	v_pk_mul_f32 v[30:31], v[6:7], v[66:67]
	v_mfma_f32_32x32x16_bf16 v[34:49], v[14:17], v[2:5], v[34:49]
	s_waitcnt lgkmcnt(0)
	v_mul_f32_e32 v10, v10, v70
	v_mul_f32_e32 v11, v11, v71
	v_mul_f32_e32 v2, v8, v68
	v_mul_f32_e32 v3, v9, v69
	v_pk_mul_f32 v[4:5], v[12:13], v[72:73]
	v_pk_fma_f32 v[6:7], v[6:7], v[66:67], v[10:11]
	v_pk_fma_f32 v[8:9], v[8:9], v[68:69], v[4:5]
	v_pk_add_f32 v[92:93], v[6:7], v[92:93]
	v_cvt_pk_bf16_f32 v3, v2, v3
	v_pk_add_f32 v[90:91], v[8:9], v[32:33]
	v_cvt_pk_bf16_f32 v5, v4, v5
	v_cvt_pk_bf16_f32 v4, v10, v11
	ds_read_b128 v[26:29], v213 offset:36864
	ds_read_b128 v[6:9], v213 offset:16384
	v_cvt_pk_bf16_f32 v2, v30, v31
	ds_read_b128 v[98:101], v213 offset:25600
	ds_read_b128 v[102:105], v213 offset:37888
	v_mfma_f32_32x32x16_bf16 v[50:65], v[14:17], v[2:5], v[50:65]
	ds_read_b128 v[2:5], v213 offset:17408
	ds_read_b128 v[30:33], v213 offset:24576
	s_waitcnt lgkmcnt(4)
	v_pk_mul_f32 v[12:13], v[6:7], v[18:19]
	v_pk_mul_f32 v[10:11], v[8:9], v[20:21]
	s_waitcnt lgkmcnt(1)
	v_pk_mul_f32 v[14:15], v[2:3], v[22:23]
	v_pk_mul_f32 v[22:23], v[98:99], v[22:23]
	v_pk_fma_f32 v[112:113], v[6:7], v[18:19], v[14:15]
	s_waitcnt lgkmcnt(0)
	v_pk_mul_f32 v[114:115], v[30:31], v[18:19]
	v_pk_fma_f32 v[118:119], v[30:31], v[18:19], v[22:23]
	v_pk_mul_f32 v[4:5], v[4:5], v[24:25]
	v_pk_mul_f32 v[106:107], v[32:33], v[20:21]
	v_pk_mul_f32 v[24:25], v[100:101], v[24:25]
	ds_read_b128 v[98:101], v213 offset:18432
	v_cvt_pk_bf16_f32 v19, v106, v107
	ds_read_b128 v[106:109], v213 offset:19456
	v_pk_fma_f32 v[110:111], v[8:9], v[20:21], v[4:5]
	v_cvt_pk_bf16_f32 v5, v4, v5
	v_cvt_pk_bf16_f32 v3, v10, v11
	v_cvt_pk_bf16_f32 v4, v14, v15
	s_waitcnt lgkmcnt(0)
	v_pk_mul_f32 v[106:107], v[106:107], v[86:87]
	v_cvt_pk_bf16_f32 v2, v12, v13
	v_pk_mul_f32 v[120:121], v[98:99], v[82:83]
	v_pk_mul_f32 v[108:109], v[108:109], v[88:89]
	v_pk_fma_f32 v[98:99], v[98:99], v[82:83], v[106:107]
	v_mfma_f32_32x32x16_bf16 v[2:17], v[26:29], v[2:5], 0
	v_cvt_pk_bf16_f32 v18, v114, v115
	v_mul_f32_e32 v114, v100, v84
	v_mul_f32_e32 v115, v101, v85
	v_fma_f32 v100, v100, v84, v108
	v_fma_f32 v101, v101, v85, v109
	v_pk_add_f32 v[124:125], v[98:99], v[112:113]
	v_pk_add_f32 v[122:123], v[100:101], v[110:111]
	v_cvt_pk_bf16_f32 v101, v108, v109
	v_cvt_pk_bf16_f32 v100, v106, v107
	ds_read_b128 v[106:109], v213 offset:26624
	v_pk_fma_f32 v[116:117], v[32:33], v[20:21], v[24:25]
	v_cvt_pk_bf16_f32 v21, v24, v25
	v_cvt_pk_bf16_f32 v20, v22, v23
	ds_read_b128 v[110:113], v213 offset:27648
	v_cvt_pk_bf16_f32 v99, v114, v115
	v_mfma_f32_32x32x16_bf16 v[18:33], v[26:29], v[18:21], 0
	v_cvt_pk_bf16_f32 v98, v120, v121
	s_waitcnt lgkmcnt(1)
	v_mul_f32_e32 v114, v106, v82
	v_mul_f32_e32 v115, v107, v83
	s_waitcnt lgkmcnt(0)
	v_pk_mul_f32 v[86:87], v[110:111], v[86:87]
	v_pk_mul_f32 v[88:89], v[112:113], v[88:89]
	v_pk_fma_f32 v[82:83], v[106:107], v[82:83], v[86:87]
	v_mfma_f32_32x32x16_bf16 v[2:17], v[102:105], v[98:101], v[2:17]
	v_mul_f32_e32 v98, v108, v84
	v_mul_f32_e32 v99, v109, v85
	v_fma_f32 v84, v108, v84, v88
	v_fma_f32 v85, v109, v85, v89
	v_add_f32_e32 v108, v82, v118
	v_add_f32_e32 v109, v83, v119
	v_cvt_pk_bf16_f32 v83, v98, v99
	v_pk_add_f32 v[106:107], v[84:85], v[116:117]
	v_cvt_pk_bf16_f32 v85, v88, v89
	v_cvt_pk_bf16_f32 v84, v86, v87
	ds_read_b128 v[86:89], v213 offset:38912
	ds_read_b128 v[98:101], v213 offset:20480
	v_cvt_pk_bf16_f32 v82, v114, v115
	s_waitcnt lgkmcnt(0)
	v_pk_mul_f32 v[110:111], v[100:101], v[76:77]
	v_mfma_f32_32x32x16_bf16 v[18:33], v[102:105], v[82:85], v[18:33]
	ds_read_b128 v[82:85], v213 offset:21504
	ds_read_b128 v[102:105], v213 offset:28672
	v_mul_f32_e32 v112, v98, v74
	v_mul_f32_e32 v113, v99, v75
	s_waitcnt lgkmcnt(1)
	v_pk_mul_f32 v[84:85], v[84:85], v[80:81]
	v_pk_mul_f32 v[114:115], v[82:83], v[78:79]
	v_pk_fma_f32 v[82:83], v[100:101], v[76:77], v[84:85]
	v_cvt_pk_bf16_f32 v85, v84, v85
	v_pk_add_f32 v[116:117], v[82:83], v[122:123]
	v_cvt_pk_bf16_f32 v83, v110, v111
	v_cvt_pk_bf16_f32 v84, v114, v115
	v_cvt_pk_bf16_f32 v82, v112, v113
	v_pk_fma_f32 v[98:99], v[98:99], v[74:75], v[114:115]
	s_waitcnt lgkmcnt(0)
	v_pk_mul_f32 v[112:113], v[102:103], v[74:75]
	v_mfma_f32_32x32x16_bf16 v[2:17], v[86:89], v[82:85], v[2:17]
	ds_read_b128 v[82:85], v213 offset:29696
	v_add_f32_e32 v118, v98, v124
	v_add_f32_e32 v119, v99, v125
	v_mul_f32_e32 v110, v104, v76
	v_mul_f32_e32 v111, v105, v77
	ds_read_b128 v[98:101], v213 offset:39936
	s_waitcnt lgkmcnt(1)
	v_pk_mul_f32 v[78:79], v[82:83], v[78:79]
	v_pk_mul_f32 v[80:81], v[84:85], v[80:81]
	v_pk_fma_f32 v[74:75], v[102:103], v[74:75], v[78:79]
	v_pk_fma_f32 v[76:77], v[104:105], v[76:77], v[80:81]
	v_pk_add_f32 v[104:105], v[74:75], v[108:109]
	v_pk_add_f32 v[102:103], v[76:77], v[106:107]
	v_cvt_pk_bf16_f32 v77, v80, v81
	v_cvt_pk_bf16_f32 v76, v78, v79
	ds_read_b128 v[78:81], v213 offset:22528
	ds_read_b128 v[82:85], v213 offset:23552
	v_cvt_pk_bf16_f32 v75, v110, v111
	v_cvt_pk_bf16_f32 v74, v112, v113
	s_waitcnt lgkmcnt(0)
	v_pk_mul_f32 v[82:83], v[82:83], v[70:71]
	v_mfma_f32_32x32x16_bf16 v[18:33], v[86:89], v[74:77], v[18:33]
	v_mul_f32_e32 v74, v80, v68
	v_mul_f32_e32 v75, v81, v69
	v_mul_f32_e32 v76, v84, v72
	v_mul_f32_e32 v77, v85, v73
	v_mul_f32_e32 v86, v78, v66
	v_mul_f32_e32 v87, v79, v67
	v_pk_fma_f32 v[80:81], v[80:81], v[68:69], v[76:77]
	v_pk_fma_f32 v[78:79], v[78:79], v[66:67], v[82:83]
	v_cvt_pk_bf16_f32 v75, v74, v75
	v_pk_add_f32 v[88:89], v[80:81], v[116:117]
	v_pk_add_f32 v[106:107], v[78:79], v[118:119]
	ds_read_b128 v[78:81], v213 offset:30720
	v_cvt_pk_bf16_f32 v77, v76, v77
	v_cvt_pk_bf16_f32 v76, v82, v83
	ds_read_b128 v[82:85], v213 offset:31744
	v_cvt_pk_bf16_f32 v74, v86, v87
	s_waitcnt lgkmcnt(0)
	v_pk_mul_f32 v[72:73], v[84:85], v[72:73]
	v_mfma_f32_32x32x16_bf16 v[2:17], v[98:101], v[74:77], v[2:17]
	v_mul_f32_e32 v74, v80, v68
	v_mul_f32_e32 v75, v81, v69
	v_fma_f32 v68, v80, v68, v72
	v_fma_f32 v69, v81, v69, v73
	v_mul_f32_e32 v70, v82, v70
	v_mul_f32_e32 v71, v83, v71
	v_pk_add_f32 v[84:85], v[68:69], v[102:103]
	v_cvt_pk_bf16_f32 v69, v72, v73
	v_pk_mov_b32 v[72:73], v[96:97], v[94:95] op_sel:[1,0]
	v_mov_b32_e32 v97, v95
	v_pk_add_f32 v[72:73], v[72:73], v[96:97]
	v_pk_mul_f32 v[76:77], v[78:79], v[66:67]
	v_pk_fma_f32 v[66:67], v[78:79], v[66:67], v[70:71]
	v_pk_add_f32 v[72:73], v[72:73], v[72:73] op_sel:[0,1] op_sel_hi:[1,0]
	v_pk_add_f32 v[86:87], v[66:67], v[104:105]
	v_mov_b32_e32 v66, v72
	s_nop 1
	v_permlane32_swap_b32_e32 v72, v66
	v_add_f32_e32 v66, v72, v66
	v_cvt_pk_bf16_f32 v67, v74, v75
	v_rcp_f32_e32 v74, v66
	v_cvt_pk_bf16_f32 v68, v70, v71
	v_cvt_pk_bf16_f32 v66, v76, v77
	v_pk_mul_f32 v[70:71], v[46:47], v[74:75] op_sel_hi:[1,0]
	s_nop 0
	v_mfma_f32_32x32x16_bf16 v[18:33], v[98:101], v[66:69], v[18:33]
	v_mul_f32_e32 v66, v42, v74
	v_mul_f32_e32 v67, v43, v74
	v_pk_mov_b32 v[42:43], v[92:93], v[90:91] op_sel:[1,0]
	v_mov_b32_e32 v93, v91
	v_pk_add_f32 v[42:43], v[42:43], v[92:93]
	v_pk_mul_f32 v[68:69], v[44:45], v[74:75] op_sel_hi:[1,0]
	v_pk_add_f32 v[42:43], v[42:43], v[42:43] op_sel:[0,1] op_sel_hi:[1,0]
	v_pk_mov_b32 v[44:45], v[106:107], v[88:89] op_sel:[1,0]
	v_mov_b32_e32 v43, v42
	s_nop 1
	v_permlane32_swap_b32_e32 v42, v43
	v_add_f32_e32 v42, v42, v43
	v_rcp_f32_e32 v42, v42
	v_mov_b32_e32 v107, v89
	v_pk_add_f32 v[44:45], v[44:45], v[106:107]
	v_pk_mul_f32 v[72:73], v[48:49], v[74:75] op_sel_hi:[1,0]
	v_pk_add_f32 v[44:45], v[44:45], v[44:45] op_sel:[0,1] op_sel_hi:[1,0]
	v_pk_mul_f32 v[36:37], v[36:37], v[74:75] op_sel_hi:[1,0]
	v_pk_mul_f32 v[38:39], v[38:39], v[74:75] op_sel_hi:[1,0]
	v_pk_mul_f32 v[40:41], v[40:41], v[74:75] op_sel_hi:[1,0]
	v_pk_mul_f32 v[34:35], v[34:35], v[74:75] op_sel_hi:[1,0]
	v_pk_mul_f32 v[74:75], v[58:59], v[42:43] op_sel_hi:[1,0]
	v_pk_mul_f32 v[78:79], v[60:61], v[42:43] op_sel_hi:[1,0]
	v_pk_mul_f32 v[80:81], v[62:63], v[42:43] op_sel_hi:[1,0]
	v_pk_mul_f32 v[82:83], v[64:65], v[42:43] op_sel_hi:[1,0]
	v_pk_mul_f32 v[92:93], v[52:53], v[42:43] op_sel_hi:[1,0]
	v_mov_b32_e32 v43, v44
	s_nop 1
	v_permlane32_swap_b32_e32 v44, v43
	v_add_f32_e32 v43, v44, v43
	v_rcp_f32_e32 v76, v43
	v_pk_mul_f32 v[96:97], v[54:55], v[42:43] op_sel_hi:[1,0]
	v_pk_mul_f32 v[94:95], v[56:57], v[42:43] op_sel_hi:[1,0]
	v_pk_mul_f32 v[98:99], v[50:51], v[42:43] op_sel_hi:[1,0]
	v_pk_mul_f32 v[100:101], v[4:5], v[76:77] op_sel_hi:[1,0]
	v_pk_mov_b32 v[4:5], v[86:87], v[84:85] op_sel:[1,0]
	v_mov_b32_e32 v87, v85
	v_pk_add_f32 v[4:5], v[4:5], v[86:87]
	v_pk_mul_f32 v[102:103], v[6:7], v[76:77] op_sel_hi:[1,0]
	v_pk_add_f32 v[104:105], v[4:5], v[4:5] op_sel:[0,1] op_sel_hi:[1,0]
	v_cvt_pk_bf16_f32 v7, v40, v41
	ds_read_b128 v[84:87], v150 offset:52224
	ds_read_b128 v[50:53], v150 offset:35840
	ds_read_b128 v[54:57], v150 offset:36864
	ds_read_b128 v[58:61], v150 offset:37888
	ds_read_b128 v[62:65], v150 offset:38912
	v_cvt_pk_bf16_f32 v6, v38, v39
	v_cvt_pk_bf16_f32 v5, v36, v37
	v_cvt_pk_bf16_f32 v4, v34, v35
	ds_read_b128 v[88:91], v150 offset:53248
	ds_read_b128 v[34:37], v150 offset:39936
	ds_read_b128 v[38:41], v150 offset:40960
	ds_read_b128 v[42:45], v150 offset:41984
	ds_read_b128 v[46:49], v150 offset:43008
	v_cvt_pk_bf16_f32 v95, v94, v95
	v_cvt_pk_bf16_f32 v94, v96, v97
	v_cvt_pk_bf16_f32 v93, v92, v93
	v_cvt_pk_bf16_f32 v92, v98, v99
	s_waitcnt lgkmcnt(5)
	v_mfma_f32_32x32x16_bf16 v[50:65], v[84:87], v[4:7], v[50:65]
	v_mul_f32_e32 v10, v10, v76
	v_mul_f32_e32 v11, v11, v76
	v_mul_f32_e32 v12, v12, v76
	v_mul_f32_e32 v13, v13, v76
	v_mul_f32_e32 v8, v8, v76
	v_mul_f32_e32 v9, v9, v76
	v_mov_b32_e32 v77, v104
	s_nop 1
	v_permlane32_swap_b32_e32 v104, v77
	v_cvt_pk_bf16_f32 v73, v72, v73
	s_waitcnt lgkmcnt(0)
	v_mfma_f32_32x32x16_bf16 v[34:49], v[84:87], v[92:95], v[34:49]
	v_cvt_pk_bf16_f32 v72, v70, v71
	v_cvt_pk_bf16_f32 v70, v66, v67
	v_add_f32_e32 v66, v104, v77
	v_cvt_pk_bf16_f32 v71, v68, v69
	v_rcp_f32_e32 v104, v66
	v_cvt_pk_bf16_f32 v69, v82, v83
	v_cvt_pk_bf16_f32 v68, v80, v81
	v_cvt_pk_bf16_f32 v67, v78, v79
	v_cvt_pk_bf16_f32 v66, v74, v75
	ds_read_b128 v[78:81], v150 offset:54272
	v_mfma_f32_32x32x16_bf16 v[50:65], v[88:91], v[70:73], v[50:65]
	v_mul_f32_e32 v2, v2, v76
	v_mul_f32_e32 v3, v3, v76
	v_mul_f32_e32 v20, v20, v104
	v_mul_f32_e32 v21, v21, v104
	v_cvt_pk_bf16_f32 v85, v8, v9
	v_cvt_pk_bf16_f32 v82, v2, v3
	v_pk_mul_f32 v[2:3], v[22:23], v[104:105] op_sel_hi:[1,0]
	v_pk_mul_f32 v[8:9], v[24:25], v[104:105] op_sel_hi:[1,0]
	v_pk_mul_f32 v[18:19], v[18:19], v[104:105] op_sel_hi:[1,0]
	v_mfma_f32_32x32x16_bf16 v[34:49], v[88:91], v[66:69], v[34:49]
	v_cvt_pk_bf16_f32 v84, v102, v103
	v_cvt_pk_bf16_f32 v83, v100, v101
	ds_read_b128 v[86:89], v150 offset:55296
	v_cvt_pk_bf16_f32 v99, v8, v9
	v_cvt_pk_bf16_f32 v98, v2, v3
	v_cvt_pk_bf16_f32 v97, v20, v21
	v_cvt_pk_bf16_f32 v96, v18, v19
	s_waitcnt lgkmcnt(1)
	v_mfma_f32_32x32x16_bf16 v[50:65], v[78:81], v[82:85], v[50:65]
	v_mul_f32_e32 v2, v14, v76
	v_mul_f32_e32 v3, v15, v76
	v_mul_f32_e32 v8, v16, v76
	v_mul_f32_e32 v9, v17, v76
	v_mul_f32_e32 v14, v26, v104
	v_mul_f32_e32 v15, v27, v104
	v_cvt_pk_bf16_f32 v77, v8, v9
	v_cvt_pk_bf16_f32 v76, v2, v3
	v_cvt_pk_bf16_f32 v74, v10, v11
	v_pk_mul_f32 v[2:3], v[28:29], v[104:105] op_sel_hi:[1,0]
	v_mfma_f32_32x32x16_bf16 v[34:49], v[78:81], v[96:99], v[34:49]
	v_mul_f32_e32 v8, v30, v104
	v_mul_f32_e32 v9, v31, v104
	v_mul_f32_e32 v10, v32, v104
	v_mul_f32_e32 v11, v33, v104
	v_cvt_pk_bf16_f32 v75, v12, v13
	v_cvt_pk_bf16_f32 v81, v10, v11
	v_cvt_pk_bf16_f32 v80, v8, v9
	v_cvt_pk_bf16_f32 v79, v2, v3
	v_cvt_pk_bf16_f32 v78, v14, v15
	s_waitcnt lgkmcnt(0)
	v_mfma_f32_32x32x16_bf16 v[50:65], v[86:89], v[74:77], v[50:65]
	v_mfma_f32_32x32x16_bf16 v[34:49], v[86:89], v[78:81], v[34:49]
	ds_read_b128 v[86:89], v150 offset:56320
	ds_read_b128 v[18:21], v150 offset:44032
	ds_read_b128 v[22:25], v150 offset:45056
	ds_read_b128 v[26:29], v150 offset:46080
	ds_read_b128 v[30:33], v150 offset:47104
	ds_read_b128 v[100:103], v150 offset:57344
	s_waitcnt lgkmcnt(1)
	v_mfma_f32_32x32x16_bf16 v[18:33], v[86:89], v[4:7], v[18:33]
	ds_read_b128 v[2:5], v150 offset:48128
	ds_read_b128 v[6:9], v150 offset:49152
	ds_read_b128 v[10:13], v150 offset:50176
	ds_read_b128 v[14:17], v150 offset:51200
	s_waitcnt lgkmcnt(0)
	v_mfma_f32_32x32x16_bf16 v[2:17], v[86:89], v[92:95], v[2:17]
	v_mfma_f32_32x32x16_bf16 v[18:33], v[100:103], v[70:73], v[18:33]
	v_mfma_f32_32x32x16_bf16 v[2:17], v[100:103], v[66:69], v[2:17]
	ds_read_b128 v[66:69], v150 offset:58368
	ds_read_b128 v[70:73], v150 offset:59392
	s_waitcnt lgkmcnt(1)
	v_mfma_f32_32x32x16_bf16 v[18:33], v[66:69], v[82:85], v[18:33]
	v_mfma_f32_32x32x16_bf16 v[2:17], v[66:69], v[96:99], v[2:17]
	s_waitcnt lgkmcnt(0)
	v_mfma_f32_32x32x16_bf16 v[18:33], v[70:73], v[74:77], v[18:33]
	v_mfma_f32_32x32x16_bf16 v[2:17], v[70:73], v[78:81], v[2:17]
	s_nop 10
	v_mul_f32_e32 v66, v22, v22
	v_mul_f32_e32 v67, v23, v23
	v_mul_f32_e32 v68, v30, v30
	v_mul_f32_e32 v69, v31, v31
	v_mul_f32_e32 v70, v24, v24
	v_mul_f32_e32 v71, v25, v25
	v_pk_mul_f32 v[72:73], v[32:33], v[32:33]
	v_pk_mul_f32 v[74:75], v[20:21], v[20:21]
	v_pk_mul_f32 v[76:77], v[28:29], v[28:29]
	v_pk_mul_f32 v[78:79], v[26:27], v[26:27]
	v_pk_mul_f32 v[80:81], v[18:19], v[18:19]
	v_pk_fma_f32 v[78:79], v[58:59], v[58:59], v[78:79]
	v_pk_fma_f32 v[76:77], v[60:61], v[60:61], v[76:77]
	v_pk_fma_f32 v[74:75], v[52:53], v[52:53], v[74:75]
	v_pk_fma_f32 v[72:73], v[64:65], v[64:65], v[72:73]
	v_pk_fma_f32 v[70:71], v[56:57], v[56:57], v[70:71]
	v_pk_fma_f32 v[68:69], v[62:63], v[62:63], v[68:69]
	v_pk_fma_f32 v[66:67], v[54:55], v[54:55], v[66:67]
	v_pk_fma_f32 v[80:81], v[50:51], v[50:51], v[80:81]
	v_pk_add_f32 v[66:67], v[66:67], v[68:69]
	v_pk_add_f32 v[68:69], v[70:71], v[72:73]
	v_pk_add_f32 v[70:71], v[74:75], v[76:77]
	v_pk_add_f32 v[72:73], v[80:81], v[78:79]
	v_pk_add_f32 v[68:69], v[70:71], v[68:69]
	v_pk_add_f32 v[66:67], v[72:73], v[66:67]
	v_pk_mul_f32 v[72:73], v[14:15], v[14:15]
	v_pk_mov_b32 v[70:71], v[66:67], v[68:69] op_sel:[1,0]
	v_mov_b32_e32 v67, v69
	v_pk_add_f32 v[66:67], v[70:71], v[66:67]
	v_pk_mul_f32 v[70:71], v[6:7], v[6:7]
	v_pk_mul_f32 v[74:75], v[8:9], v[8:9]
	v_pk_mul_f32 v[76:77], v[16:17], v[16:17]
	v_pk_mul_f32 v[78:79], v[4:5], v[4:5]
	v_pk_mul_f32 v[80:81], v[12:13], v[12:13]
	v_pk_mul_f32 v[82:83], v[10:11], v[10:11]
	v_pk_mul_f32 v[84:85], v[2:3], v[2:3]
	v_pk_fma_f32 v[82:83], v[42:43], v[42:43], v[82:83]
	v_pk_fma_f32 v[80:81], v[44:45], v[44:45], v[80:81]
	v_pk_fma_f32 v[78:79], v[36:37], v[36:37], v[78:79]
	v_pk_fma_f32 v[76:77], v[48:49], v[48:49], v[76:77]
	v_pk_fma_f32 v[74:75], v[40:41], v[40:41], v[74:75]
	v_pk_fma_f32 v[72:73], v[46:47], v[46:47], v[72:73]
	v_pk_fma_f32 v[70:71], v[38:39], v[38:39], v[70:71]
	v_pk_fma_f32 v[84:85], v[34:35], v[34:35], v[84:85]
	v_pk_add_f32 v[70:71], v[70:71], v[72:73]
	v_pk_add_f32 v[72:73], v[74:75], v[76:77]
	v_pk_add_f32 v[74:75], v[78:79], v[80:81]
	v_pk_add_f32 v[76:77], v[84:85], v[82:83]
	v_pk_add_f32 v[72:73], v[74:75], v[72:73]
	v_pk_add_f32 v[70:71], v[76:77], v[70:71]
	v_pk_add_f32 v[66:67], v[66:67], v[66:67] op_sel:[0,1] op_sel_hi:[1,0]
	v_pk_mov_b32 v[74:75], v[70:71], v[72:73] op_sel:[1,0]
	v_mov_b32_e32 v71, v73
	v_pk_add_f32 v[70:71], v[74:75], v[70:71]
	v_mov_b32_e32 v69, v66
	v_pk_add_f32 v[70:71], v[70:71], v[70:71] op_sel:[0,1] op_sel_hi:[1,0]
	s_nop 0
	v_permlane32_swap_b32_e32 v66, v69
	v_mov_b32_e32 v68, v70
	s_nop 1
	v_permlane32_swap_b32_e32 v70, v68
	v_mov_b32_e32 v71, v66
	v_pk_add_f32 v[66:67], v[70:71], v[68:69]
	v_pk_fma_f32 v[66:67], v[66:67], s[0:1], v[152:153] op_sel_hi:[1,0,0]
	s_mov_b32 s1, 0x800000
	v_mul_f32_e32 v68, 0x4b800000, v67
	v_cmp_gt_f32_e32 vcc, s1, v67
	s_nop 1
	v_cndmask_b32_e32 v67, v67, v68, vcc
	v_rsq_f32_e32 v67, v67
	s_nop 0
	v_mul_f32_e32 v68, 0x45800000, v67
	v_cndmask_b32_e32 v68, v67, v68, vcc
	v_pk_mul_f32 v[158:159], v[50:51], v[68:69] op_sel_hi:[1,0]
	v_pk_mul_f32 v[50:51], v[18:19], v[68:69] op_sel_hi:[1,0]
	v_mul_f32_e32 v18, 0x4b800000, v66
	v_cmp_gt_f32_e32 vcc, s1, v66
	v_pk_mul_f32 v[80:81], v[60:61], v[68:69] op_sel_hi:[1,0]
	v_pk_mul_f32 v[60:61], v[28:29], v[68:69] op_sel_hi:[1,0]
	v_cndmask_b32_e32 v18, v66, v18, vcc
	v_rsq_f32_e32 v18, v18
	v_pk_mul_f32 v[78:79], v[58:59], v[68:69] op_sel_hi:[1,0]
	v_pk_mul_f32 v[160:161], v[52:53], v[68:69] op_sel_hi:[1,0]
	v_pk_mul_f32 v[82:83], v[54:55], v[68:69] op_sel_hi:[1,0]
	v_mul_f32_e32 v19, 0x45800000, v18
	v_cndmask_b32_e32 v28, v18, v19, vcc
	v_pk_mul_f32 v[168:169], v[56:57], v[68:69] op_sel_hi:[1,0]
	v_pk_mul_f32 v[58:59], v[26:27], v[68:69] op_sel_hi:[1,0]
	v_pk_mul_f32 v[52:53], v[20:21], v[68:69] op_sel_hi:[1,0]
	v_pk_mul_f32 v[54:55], v[22:23], v[68:69] op_sel_hi:[1,0]
	v_pk_mul_f32 v[56:57], v[24:25], v[68:69] op_sel_hi:[1,0]
	v_pk_mul_f32 v[18:19], v[42:43], v[28:29] op_sel_hi:[1,0]
	v_pk_mul_f32 v[20:21], v[44:45], v[28:29] op_sel_hi:[1,0]
	v_pk_mul_f32 v[22:23], v[46:47], v[28:29] op_sel_hi:[1,0]
	v_pk_mul_f32 v[26:27], v[48:49], v[28:29] op_sel_hi:[1,0]
	v_pk_mul_f32 v[162:163], v[34:35], v[28:29] op_sel_hi:[1,0]
	v_pk_mul_f32 v[164:165], v[36:37], v[28:29] op_sel_hi:[1,0]
	v_pk_mul_f32 v[166:167], v[38:39], v[28:29] op_sel_hi:[1,0]
	v_pk_mul_f32 v[24:25], v[40:41], v[28:29] op_sel_hi:[1,0]
	v_pk_mul_f32 v[104:105], v[2:3], v[28:29] op_sel_hi:[1,0]
	v_pk_mul_f32 v[112:113], v[4:5], v[28:29] op_sel_hi:[1,0]
	ds_read_b128 v[2:5], v150 offset:60416
	ds_read_b128 v[34:37], v174 offset:32768
	ds_read_b128 v[38:41], v174 offset:32800
	ds_read_b128 v[42:45], v174 offset:32832
	ds_read_b128 v[46:49], v174 offset:32864
	v_cvt_pk_bf16_f32 v129, v168, v169
	v_cvt_pk_bf16_f32 v128, v82, v83
	v_cvt_pk_bf16_f32 v127, v160, v161
	v_cvt_pk_bf16_f32 v126, v158, v159
	v_cvt_pk_bf16_f32 v137, v24, v25
	v_cvt_pk_bf16_f32 v136, v166, v167
	v_cvt_pk_bf16_f32 v135, v164, v165
	s_waitcnt lgkmcnt(0)
	v_mfma_f32_32x32x16_bf16 v[86:101], v[2:5], v[126:129], v[34:49]
	v_cvt_pk_bf16_f32 v134, v162, v163
	v_mul_f32_e32 v84, v62, v68
	v_mul_f32_e32 v85, v63, v68
	v_mul_f32_e32 v170, v64, v68
	v_mul_f32_e32 v171, v65, v68
	v_pk_mul_f32 v[62:63], v[30:31], v[68:69] op_sel_hi:[1,0]
	v_pk_mul_f32 v[64:65], v[32:33], v[68:69] op_sel_hi:[1,0]
	v_pk_mul_f32 v[116:117], v[6:7], v[28:29] op_sel_hi:[1,0]
	v_pk_mul_f32 v[154:155], v[8:9], v[28:29] op_sel_hi:[1,0]
	v_mfma_f32_32x32x16_bf16 v[34:49], v[2:5], v[134:137], v[34:49]
	ds_read_b128 v[6:9], v150 offset:61440
	ds_read_b128 v[66:69], v174 offset:32896
	ds_read_b128 v[106:109], v150 offset:64512
	v_cvt_pk_bf16_f32 v125, v170, v171
	v_cvt_pk_bf16_f32 v124, v84, v85
	v_cvt_pk_bf16_f32 v123, v80, v81
	v_cvt_pk_bf16_f32 v122, v78, v79
	v_cvt_pk_bf16_f32 v149, v26, v27
	v_cvt_pk_bf16_f32 v148, v22, v23
	v_cvt_pk_bf16_f32 v147, v20, v21
	v_cvt_pk_bf16_f32 v146, v18, v19
	s_waitcnt lgkmcnt(2)
	v_mfma_f32_32x32x16_bf16 v[86:101], v[6:9], v[122:125], v[86:101]
	v_mul_f32_e32 v102, v10, v28
	v_mul_f32_e32 v103, v11, v28
	v_mul_f32_e32 v110, v12, v28
	v_mul_f32_e32 v111, v13, v28
	v_mul_f32_e32 v114, v14, v28
	v_mul_f32_e32 v115, v15, v28
	v_pk_mul_f32 v[156:157], v[16:17], v[28:29] op_sel_hi:[1,0]
	ds_read_b128 v[176:179], v174 offset:33536
	ds_read_b128 v[180:183], v174 offset:33568
	ds_read_b128 v[184:187], v174 offset:33600
	ds_read_b128 v[28:31], v174 offset:33632
	ds_read_b128 v[188:191], v174 offset:33792
	ds_read_b128 v[192:195], v174 offset:33824
	ds_read_b128 v[196:199], v174 offset:33856
	ds_read_b128 v[200:203], v174 offset:33888
	ds_read_b128 v[204:207], v150 offset:62464
	v_cvt_pk_bf16_f32 v133, v56, v57
	v_mfma_f32_32x32x16_bf16 v[34:49], v[6:9], v[146:149], v[34:49]
	v_cvt_pk_bf16_f32 v132, v54, v55
	v_cvt_pk_bf16_f32 v131, v52, v53
	v_cvt_pk_bf16_f32 v130, v50, v51
	ds_read_b128 v[70:73], v174 offset:33664
	ds_read_b128 v[74:77], v174 offset:33920
	ds_read_b128 v[208:211], v150 offset:63488
	v_cvt_pk_bf16_f32 v145, v154, v155
	v_cvt_pk_bf16_f32 v144, v116, v117
	v_cvt_pk_bf16_f32 v143, v112, v113
	v_cvt_pk_bf16_f32 v142, v104, v105
	s_waitcnt lgkmcnt(3)
	v_mfma_f32_32x32x16_bf16 v[86:101], v[204:207], v[130:133], v[86:101]
	v_cvt_pk_bf16_f32 v121, v64, v65
	v_cvt_pk_bf16_f32 v120, v62, v63
	v_cvt_pk_bf16_f32 v119, v60, v61
	v_cvt_pk_bf16_f32 v118, v58, v59
	v_cvt_pk_bf16_f32 v141, v156, v157
	v_cvt_pk_bf16_f32 v140, v114, v115
	v_cvt_pk_bf16_f32 v139, v110, v111
	v_mfma_f32_32x32x16_bf16 v[34:49], v[204:207], v[142:145], v[34:49]
	v_cvt_pk_bf16_f32 v138, v102, v103
	v_fma_f32 v16, v30, v170, v202
	v_fma_f32 v17, v31, v171, v203
	v_fma_f32 v14, v28, v84, v200
	v_fma_f32 v15, v29, v85, v201
	v_pk_fma_f32 v[12:13], v[186:187], v[80:81], v[198:199]
	v_pk_fma_f32 v[10:11], v[184:185], v[78:79], v[196:197]
	v_pk_fma_f32 v[8:9], v[182:183], v[168:169], v[194:195]
	s_waitcnt lgkmcnt(0)
	v_mfma_f32_32x32x16_bf16 v[86:101], v[208:211], v[118:121], v[86:101]
	v_fma_f32 v6, v180, v82, v192
	v_fma_f32 v7, v181, v83, v193
	ds_read_b128 v[78:81], v174 offset:33760
	ds_read_b128 v[82:85], v174 offset:33248
	v_fma_f32 v4, v178, v160, v190
	v_fma_f32 v5, v179, v161, v191
	v_pk_fma_f32 v[2:3], v[176:177], v[158:159], v[188:189]
	v_pk_fma_f32 v[32:33], v[30:31], v[26:27], v[202:203]
	v_pk_fma_f32 v[30:31], v[28:29], v[22:23], v[200:201]
	v_pk_fma_f32 v[28:29], v[186:187], v[20:21], v[198:199]
	v_pk_fma_f32 v[26:27], v[184:185], v[18:19], v[196:197]
	v_pk_fma_f32 v[24:25], v[182:183], v[24:25], v[194:195]
	v_pk_fma_f32 v[22:23], v[180:181], v[166:167], v[192:193]
	v_pk_fma_f32 v[20:21], v[178:179], v[164:165], v[190:191]
	v_pk_fma_f32 v[18:19], v[176:177], v[162:163], v[188:189]
	ds_read_b128 v[158:161], v174 offset:33696
	ds_read_b128 v[162:165], v174 offset:33728
	ds_read_b128 v[166:169], v174 offset:33952
	ds_read_b128 v[176:179], v174 offset:33984
	ds_read_b128 v[180:183], v174 offset:34016
	ds_read_b128 v[184:187], v212 offset:11264
	v_mfma_f32_32x32x16_bf16 v[34:49], v[208:211], v[138:141], v[34:49]
	v_cvt_pk_bf16_f32 v86, v86, v87
	v_cvt_pk_bf16_f32 v87, v88, v89
	v_cvt_pk_bf16_f32 v88, v90, v91
	v_cvt_pk_bf16_f32 v89, v92, v93
	ds_read_b128 v[90:93], v212 offset:12288
	v_pk_max_i16 v86, v86, 0
	v_pk_max_i16 v87, v87, 0
	v_pk_max_i16 v88, v88, 0
	v_pk_max_i16 v89, v89, 0
	s_nop 1
	s_nop 0
	v_cvt_pk_bf16_f32 v188, v34, v35
	v_cvt_pk_bf16_f32 v189, v36, v37
	v_cvt_pk_bf16_f32 v190, v38, v39
	v_cvt_pk_bf16_f32 v191, v40, v41
	s_waitcnt lgkmcnt(1)
	v_mfma_f32_32x32x16_bf16 v[2:17], v[184:187], v[86:89], v[2:17]
	v_pk_max_i16 v188, v188, 0
	v_pk_max_i16 v189, v189, 0
	v_pk_max_i16 v190, v190, 0
	v_pk_max_i16 v191, v191, 0
	v_cvt_pk_bf16_f32 v94, v94, v95
	v_cvt_pk_bf16_f32 v95, v96, v97
	v_cvt_pk_bf16_f32 v96, v98, v99
	v_cvt_pk_bf16_f32 v97, v100, v101
	v_cvt_pk_bf16_f32 v98, v42, v43
	v_cvt_pk_bf16_f32 v99, v44, v45
	v_mfma_f32_32x32x16_bf16 v[18:33], v[184:187], v[188:191], v[18:33]
	ds_read_b128 v[184:187], v212 offset:19456
	v_cvt_pk_bf16_f32 v100, v46, v47
	v_cvt_pk_bf16_f32 v101, v48, v49
	v_fma_f32 v64, v80, v64, v182
	v_fma_f32 v65, v81, v65, v183
	v_pk_fma_f32 v[62:63], v[78:79], v[62:63], v[180:181]
	v_pk_fma_f32 v[60:61], v[164:165], v[60:61], v[178:179]
	v_pk_fma_f32 v[58:59], v[162:163], v[58:59], v[176:177]
	v_pk_max_i16 v94, v94, 0
	v_pk_max_i16 v95, v95, 0
	v_pk_max_i16 v96, v96, 0
	v_pk_max_i16 v97, v97, 0
	v_pk_max_i16 v98, v98, 0
	v_pk_max_i16 v99, v99, 0
	v_pk_max_i16 v100, v100, 0
	v_pk_max_i16 v101, v101, 0
	v_pk_fma_f32 v[56:57], v[160:161], v[56:57], v[168:169]
	s_waitcnt lgkmcnt(1)
	v_mfma_f32_32x32x16_bf16 v[2:17], v[90:93], v[94:97], v[2:17]
	v_fma_f32 v54, v158, v54, v166
	v_fma_f32 v55, v159, v55, v167
	v_fma_f32 v52, v72, v52, v76
	v_fma_f32 v53, v73, v53, v77
	v_fma_f32 v50, v70, v50, v74
	v_fma_f32 v51, v71, v51, v75
	v_pk_fma_f32 v[48:49], v[80:81], v[156:157], v[182:183]
	v_pk_fma_f32 v[46:47], v[78:79], v[114:115], v[180:181]
	v_pk_fma_f32 v[44:45], v[164:165], v[110:111], v[178:179]
	v_pk_fma_f32 v[42:43], v[162:163], v[102:103], v[176:177]
	v_mfma_f32_32x32x16_bf16 v[18:33], v[90:93], v[98:101], v[18:33]
	ds_read_b128 v[90:93], v212 offset:20480
	v_fma_f32 v40, v160, v154, v168
	v_fma_f32 v41, v161, v155, v169
	v_fma_f32 v38, v158, v116, v166
	v_fma_f32 v39, v159, v117, v167
	v_pk_fma_f32 v[36:37], v[72:73], v[112:113], v[76:77]
	v_pk_fma_f32 v[34:35], v[70:71], v[104:105], v[74:75]
	s_waitcnt lgkmcnt(1)
	v_mfma_f32_32x32x16_bf16 v[50:65], v[184:187], v[86:89], v[50:65]
	ds_read_b128 v[70:73], v174 offset:32928
	ds_read_b128 v[74:77], v174 offset:32960
	ds_read_b128 v[78:81], v174 offset:32992
	ds_read_b128 v[86:89], v174 offset:33024
	ds_read_b128 v[110:113], v212 offset:1024
	v_mfma_f32_32x32x16_bf16 v[34:49], v[184:187], v[188:191], v[34:49]
	s_waitcnt lgkmcnt(5)
	v_mfma_f32_32x32x16_bf16 v[50:65], v[90:93], v[94:97], v[50:65]
	v_mfma_f32_32x32x16_bf16 v[34:49], v[90:93], v[98:101], v[34:49]
	s_waitcnt lgkmcnt(2)
	v_mfma_f32_32x32x16_bf16 v[90:105], v[106:109], v[126:129], v[66:81]
	v_mfma_f32_32x32x16_bf16 v[66:81], v[106:109], v[134:137], v[66:81]
	ds_read_b128 v[106:109], v212 offset:0
	s_waitcnt lgkmcnt(0)
	v_mfma_f32_32x32x16_bf16 v[90:105], v[106:109], v[122:125], v[90:105]
	v_mfma_f32_32x32x16_bf16 v[66:81], v[106:109], v[146:149], v[66:81]
	ds_read_b128 v[106:109], v212 offset:2048
	v_mfma_f32_32x32x16_bf16 v[90:105], v[110:113], v[130:133], v[90:105]
	v_mfma_f32_32x32x16_bf16 v[66:81], v[110:113], v[142:145], v[66:81]
	ds_read_b128 v[110:113], v212 offset:13312
	s_waitcnt lgkmcnt(1)
	v_mfma_f32_32x32x16_bf16 v[90:105], v[106:109], v[118:121], v[90:105]
	v_mfma_f32_32x32x16_bf16 v[66:81], v[106:109], v[138:141], v[66:81]
	s_nop 10
	v_cvt_pk_bf16_f32 v90, v90, v91
	v_cvt_pk_bf16_f32 v91, v92, v93
	v_cvt_pk_bf16_f32 v92, v94, v95
	v_cvt_pk_bf16_f32 v94, v98, v99
	v_cvt_pk_bf16_f32 v95, v100, v101
	ds_read_b128 v[98:101], v212 offset:21504
	v_cvt_pk_bf16_f32 v66, v66, v67
	v_cvt_pk_bf16_f32 v67, v68, v69
	v_cvt_pk_bf16_f32 v68, v70, v71
	v_cvt_pk_bf16_f32 v93, v96, v97
	v_cvt_pk_bf16_f32 v69, v72, v73
	ds_read_b128 v[70:73], v212 offset:14336
	v_pk_max_i16 v90, v90, 0
	v_pk_max_i16 v91, v91, 0
	v_pk_max_i16 v92, v92, 0
	v_pk_max_i16 v93, v93, 0
	v_pk_max_i16 v66, v66, 0
	v_pk_max_i16 v67, v67, 0
	v_pk_max_i16 v68, v68, 0
	v_pk_max_i16 v69, v69, 0
	v_cvt_pk_bf16_f32 v96, v102, v103
	s_waitcnt lgkmcnt(2)
	v_mfma_f32_32x32x16_bf16 v[2:17], v[110:113], v[90:93], v[2:17]
	v_cvt_pk_bf16_f32 v97, v104, v105
	v_cvt_pk_bf16_f32 v74, v74, v75
	v_cvt_pk_bf16_f32 v75, v76, v77
	v_cvt_pk_bf16_f32 v76, v78, v79
	v_cvt_pk_bf16_f32 v77, v80, v81
	v_pk_max_i16 v94, v94, 0
	v_pk_max_i16 v95, v95, 0
	v_pk_max_i16 v96, v96, 0
	v_pk_max_i16 v97, v97, 0
	v_pk_max_i16 v74, v74, 0
	v_pk_max_i16 v75, v75, 0
	v_pk_max_i16 v76, v76, 0
	v_pk_max_i16 v77, v77, 0
	v_mfma_f32_32x32x16_bf16 v[18:33], v[110:113], v[66:69], v[18:33]
	s_waitcnt lgkmcnt(1)
	v_mfma_f32_32x32x16_bf16 v[34:49], v[98:101], v[66:69], v[34:49]
	ds_read_b128 v[66:69], v212 offset:22528
	v_mfma_f32_32x32x16_bf16 v[50:65], v[98:101], v[90:93], v[50:65]
	s_waitcnt lgkmcnt(1)
	v_mfma_f32_32x32x16_bf16 v[2:17], v[70:73], v[94:97], v[2:17]
	v_mfma_f32_32x32x16_bf16 v[18:33], v[70:73], v[74:77], v[18:33]
	ds_read_b128 v[78:81], v212 offset:3072
	s_waitcnt lgkmcnt(1)
	v_mfma_f32_32x32x16_bf16 v[50:65], v[66:69], v[94:97], v[50:65]
	ds_read_b128 v[90:93], v174 offset:33056
	ds_read_b128 v[94:97], v174 offset:33088
	ds_read_b128 v[98:101], v174 offset:33120
	ds_read_b128 v[70:73], v174 offset:33152
	v_mfma_f32_32x32x16_bf16 v[34:49], v[66:69], v[74:77], v[34:49]
	ds_read_b128 v[66:69], v212 offset:4096
	ds_read_b128 v[74:77], v212 offset:5120
	s_waitcnt lgkmcnt(3)
	v_mfma_f32_32x32x16_bf16 v[102:117], v[78:81], v[126:129], v[86:101]
	v_mfma_f32_32x32x16_bf16 v[86:101], v[78:81], v[134:137], v[86:101]
	s_waitcnt lgkmcnt(1)
	v_mfma_f32_32x32x16_bf16 v[86:101], v[66:69], v[146:149], v[86:101]
	v_mfma_f32_32x32x16_bf16 v[102:117], v[66:69], v[122:125], v[102:117]
	ds_read_b128 v[66:69], v212 offset:6144
	s_waitcnt lgkmcnt(1)
	v_mfma_f32_32x32x16_bf16 v[86:101], v[74:77], v[142:145], v[86:101]
	v_mfma_f32_32x32x16_bf16 v[102:117], v[74:77], v[130:133], v[102:117]
	ds_read_b128 v[74:77], v212 offset:15360
	s_waitcnt lgkmcnt(1)
	v_mfma_f32_32x32x16_bf16 v[86:101], v[66:69], v[138:141], v[86:101]
	v_mfma_f32_32x32x16_bf16 v[102:117], v[66:69], v[118:121], v[102:117]
	s_nop 10
	v_cvt_pk_bf16_f32 v78, v86, v87
	v_cvt_pk_bf16_f32 v80, v90, v91
	v_cvt_pk_bf16_f32 v79, v88, v89
	v_cvt_pk_bf16_f32 v81, v92, v93
	ds_read_b128 v[86:89], v212 offset:16384
	ds_read_b128 v[90:93], v212 offset:23552
	v_cvt_pk_bf16_f32 v66, v102, v103
	v_cvt_pk_bf16_f32 v67, v104, v105
	v_cvt_pk_bf16_f32 v68, v106, v107
	v_cvt_pk_bf16_f32 v69, v108, v109
	v_pk_max_i16 v66, v66, 0
	v_pk_max_i16 v67, v67, 0
	v_pk_max_i16 v68, v68, 0
	v_pk_max_i16 v69, v69, 0
	v_pk_max_i16 v78, v78, 0
	v_pk_max_i16 v79, v79, 0
	v_pk_max_i16 v80, v80, 0
	v_pk_max_i16 v81, v81, 0
	v_cvt_pk_bf16_f32 v94, v94, v95
	s_waitcnt lgkmcnt(2)
	v_mfma_f32_32x32x16_bf16 v[18:33], v[74:77], v[78:81], v[18:33]
	v_cvt_pk_bf16_f32 v95, v96, v97
	v_cvt_pk_bf16_f32 v96, v98, v99
	v_cvt_pk_bf16_f32 v97, v100, v101
	v_pk_max_i16 v94, v94, 0
	v_pk_max_i16 v95, v95, 0
	v_pk_max_i16 v96, v96, 0
	v_pk_max_i16 v97, v97, 0
	v_mfma_f32_32x32x16_bf16 v[2:17], v[74:77], v[66:69], v[2:17]
	v_cvt_pk_bf16_f32 v74, v110, v111
	v_cvt_pk_bf16_f32 v75, v112, v113
	v_cvt_pk_bf16_f32 v76, v114, v115
	v_cvt_pk_bf16_f32 v77, v116, v117
	v_pk_max_i16 v74, v74, 0
	v_pk_max_i16 v75, v75, 0
	v_pk_max_i16 v76, v76, 0
	v_pk_max_i16 v77, v77, 0
	s_waitcnt lgkmcnt(0)
	v_mfma_f32_32x32x16_bf16 v[50:65], v[90:93], v[66:69], v[50:65]
	ds_read_b128 v[66:69], v212 offset:24576
	v_mfma_f32_32x32x16_bf16 v[34:49], v[90:93], v[78:81], v[34:49]
	ds_read_b128 v[102:105], v212 offset:7168
	v_mfma_f32_32x32x16_bf16 v[2:17], v[86:89], v[74:77], v[2:17]
	s_waitcnt lgkmcnt(1)
	v_mfma_f32_32x32x16_bf16 v[50:65], v[66:69], v[74:77], v[50:65]
	ds_read_b128 v[74:77], v174 offset:33184
	ds_read_b128 v[78:81], v174 offset:33216
	v_mfma_f32_32x32x16_bf16 v[34:49], v[66:69], v[94:97], v[34:49]
	ds_read_b128 v[66:69], v212 offset:8192
	v_mfma_f32_32x32x16_bf16 v[18:33], v[86:89], v[94:97], v[18:33]
	s_waitcnt lgkmcnt(1)
	v_mfma_f32_32x32x16_bf16 v[86:101], v[102:105], v[126:129], v[70:85]
	v_mfma_f32_32x32x16_bf16 v[70:85], v[102:105], v[134:137], v[70:85]
	ds_read_b128 v[102:105], v212 offset:9216
	v_lshlrev_b32_e32 v135, 2, v1
	v_add_u32_e32 v134, v172, v174
	s_waitcnt lgkmcnt(1)
	v_mfma_f32_32x32x16_bf16 v[86:101], v[66:69], v[122:125], v[86:101]
	v_mfma_f32_32x32x16_bf16 v[70:85], v[66:69], v[146:149], v[70:85]
	ds_read_b128 v[66:69], v212 offset:10240
	s_waitcnt lgkmcnt(1)
	v_mfma_f32_32x32x16_bf16 v[86:101], v[102:105], v[130:133], v[86:101]
	v_mfma_f32_32x32x16_bf16 v[70:85], v[102:105], v[142:145], v[70:85]
	ds_read_b128 v[102:105], v212 offset:17408
	s_waitcnt lgkmcnt(1)
	v_mfma_f32_32x32x16_bf16 v[86:101], v[66:69], v[118:121], v[86:101]
	v_mfma_f32_32x32x16_bf16 v[70:85], v[66:69], v[138:141], v[70:85]
	s_nop 10
	v_cvt_pk_bf16_f32 v68, v90, v91
	v_cvt_pk_bf16_f32 v69, v92, v93
	ds_read_b128 v[90:93], v212 offset:25600
	v_cvt_pk_bf16_f32 v66, v86, v87
	v_cvt_pk_bf16_f32 v67, v88, v89
	v_pk_max_i16 v66, v66, 0
	v_pk_max_i16 v67, v67, 0
	v_pk_max_i16 v68, v68, 0
	v_pk_max_i16 v69, v69, 0
	v_cvt_pk_bf16_f32 v70, v70, v71
	v_cvt_pk_bf16_f32 v71, v72, v73
	s_waitcnt lgkmcnt(1)
	v_mfma_f32_32x32x16_bf16 v[2:17], v[102:105], v[66:69], v[2:17]
	v_cvt_pk_bf16_f32 v72, v74, v75
	v_cvt_pk_bf16_f32 v73, v76, v77
	ds_read_b128 v[74:77], v212 offset:18432
	v_cvt_pk_bf16_f32 v86, v94, v95
	v_cvt_pk_bf16_f32 v87, v96, v97
	v_cvt_pk_bf16_f32 v88, v98, v99
	s_waitcnt lgkmcnt(1)
	v_mfma_f32_32x32x16_bf16 v[50:65], v[90:93], v[66:69], v[50:65]
	ds_read_b128 v[66:69], v212 offset:26624
	v_cvt_pk_bf16_f32 v89, v100, v101
	v_pk_max_i16 v86, v86, 0
	v_pk_max_i16 v87, v87, 0
	v_pk_max_i16 v88, v88, 0
	v_pk_max_i16 v89, v89, 0
	v_pk_max_i16 v70, v70, 0
	v_pk_max_i16 v71, v71, 0
	v_pk_max_i16 v72, v72, 0
	v_pk_max_i16 v73, v73, 0
	v_cvt_pk_bf16_f32 v78, v78, v79
	v_cvt_pk_bf16_f32 v79, v80, v81
	s_waitcnt lgkmcnt(1)
	v_mfma_f32_32x32x16_bf16 v[2:17], v[74:77], v[86:89], v[2:17]
	v_cvt_pk_bf16_f32 v80, v82, v83
	v_cvt_pk_bf16_f32 v81, v84, v85
	v_pk_max_i16 v78, v78, 0
	v_pk_max_i16 v79, v79, 0
	v_pk_max_i16 v80, v80, 0
	v_pk_max_i16 v81, v81, 0
	s_waitcnt lgkmcnt(0)
	v_mfma_f32_32x32x16_bf16 v[50:65], v[66:69], v[86:89], v[50:65]
	v_mfma_f32_32x32x16_bf16 v[34:49], v[90:93], v[70:73], v[34:49]
	s_nop 10
	v_add_f32_e32 v130, v10, v58
	v_add_f32_e32 v131, v11, v59
	v_add_f32_e32 v132, v12, v60
	v_add_f32_e32 v133, v13, v61
	v_add_f32_e32 v138, v4, v52
	v_add_f32_e32 v139, v5, v53
	v_pk_add_f32 v[140:141], v[16:17], v[64:65]
	v_pk_add_f32 v[142:143], v[8:9], v[56:57]
	v_pk_add_f32 v[144:145], v[14:15], v[62:63]
	v_pk_add_f32 v[146:147], v[6:7], v[54:55]
	v_mfma_f32_32x32x16_bf16 v[18:33], v[102:105], v[70:73], v[18:33]
	ds_read2st64_b32 v[70:71], v135 offset0:133 offset1:134
	v_add_f32_e32 v148, v2, v50
	v_add_f32_e32 v149, v3, v51
	v_add_f32_e32 v144, v146, v144
	v_add_f32_e32 v145, v147, v145
	v_pk_add_f32 v[140:141], v[142:143], v[140:141]
	v_pk_add_f32 v[132:133], v[138:139], v[132:133]
	v_pk_add_f32 v[130:131], v[148:149], v[130:131]
	v_pk_add_f32 v[132:133], v[132:133], v[140:141]
	v_pk_add_f32 v[130:131], v[130:131], v[144:145]
	v_mfma_f32_32x32x16_bf16 v[34:49], v[66:69], v[78:81], v[34:49]
	v_pk_mov_b32 v[138:139], v[130:131], v[132:133] op_sel:[1,0]
	v_mov_b32_e32 v131, v133
	s_waitcnt vmcnt(0) lgkmcnt(0)
	v_mul_f32_e32 v66, v175, v70
	v_pk_add_f32 v[130:131], v[138:139], v[130:131]
	ds_write_b32 v173, v66 offset:512
	v_mul_f32_e32 v66, v175, v71
	v_pk_add_f32 v[130:131], v[130:131], v[130:131] op_sel:[0,1] op_sel_hi:[1,0]
	s_waitcnt lgkmcnt(0)
	ds_read_b128 v[102:105], v174 offset:34560
	ds_read_b128 v[98:101], v174 offset:34592
	ds_read_b128 v[110:113], v174 offset:34624
	ds_read_b128 v[106:109], v174 offset:34656
	ds_read_b128 v[114:117], v174 offset:34688
	ds_read_b128 v[122:125], v174 offset:34720
	ds_read_b128 v[118:121], v174 offset:34752
	ds_read_b128 v[126:129], v174 offset:34784
	v_mov_b32_dpp v66, v66 quad_perm:[1,0,3,2] row_mask:0xf bank_mask:0xf bound_ctrl:1
	v_mov_b32_e32 v131, v130
	v_fmac_f32_e32 v66, v175, v71
	s_nop 0
	v_permlane32_swap_b32_e32 v130, v131
	v_add_f32_dpp v66, v66, v66 quad_perm:[2,3,0,1] row_mask:0xf bank_mask:0xf bound_ctrl:1
	v_add_f32_e32 v130, v130, v131
	v_fmamk_f32 v65, v130, 0xbc800000, v65
	v_add_f32_dpp v66, v66, v66 row_half_mirror row_mask:0xf bank_mask:0xf bound_ctrl:1
	v_fmamk_f32 v64, v130, 0xbc800000, v64
	v_fmamk_f32 v63, v130, 0xbc800000, v63
	v_fmamk_f32 v62, v130, 0xbc800000, v62
	v_fmamk_f32 v61, v130, 0xbc800000, v61
	v_fmamk_f32 v60, v130, 0xbc800000, v60
	v_fmamk_f32 v59, v130, 0xbc800000, v59
	v_fmamk_f32 v58, v130, 0xbc800000, v58
	v_fmamk_f32 v57, v130, 0xbc800000, v57
	v_fmamk_f32 v56, v130, 0xbc800000, v56
	v_fmamk_f32 v55, v130, 0xbc800000, v55
	v_fmamk_f32 v54, v130, 0xbc800000, v54
	v_fmamk_f32 v53, v130, 0xbc800000, v53
	v_fmamk_f32 v52, v130, 0xbc800000, v52
	v_fmamk_f32 v51, v130, 0xbc800000, v51
	v_fmac_f32_e32 v50, 0xbc800000, v130
	v_add_f32_dpp v66, v66, v66 row_ror:8 row_mask:0xf bank_mask:0xf bound_ctrl:1
	v_fmamk_f32 v17, v130, 0xbc800000, v17
	v_fmamk_f32 v16, v130, 0xbc800000, v16
	v_fmamk_f32 v15, v130, 0xbc800000, v15
	v_fmamk_f32 v14, v130, 0xbc800000, v14
	v_fmamk_f32 v13, v130, 0xbc800000, v13
	v_fmamk_f32 v12, v130, 0xbc800000, v12
	v_fmamk_f32 v11, v130, 0xbc800000, v11
	v_fmamk_f32 v10, v130, 0xbc800000, v10
	v_fmamk_f32 v9, v130, 0xbc800000, v9
	v_fmamk_f32 v8, v130, 0xbc800000, v8
	v_fmamk_f32 v7, v130, 0xbc800000, v7
	v_fmamk_f32 v6, v130, 0xbc800000, v6
	v_fmamk_f32 v5, v130, 0xbc800000, v5
	v_fmamk_f32 v4, v130, 0xbc800000, v4
	v_fmamk_f32 v3, v130, 0xbc800000, v3
	v_fmac_f32_e32 v2, 0xbc800000, v130
	v_pk_mul_f32 v[130:131], v[54:55], v[54:55]
	v_pk_mul_f32 v[132:133], v[62:63], v[62:63]
	v_pk_mul_f32 v[138:139], v[50:51], v[50:51]
	v_pk_mul_f32 v[140:141], v[58:59], v[58:59]
	v_pk_mul_f32 v[142:143], v[56:57], v[56:57]
	v_pk_mul_f32 v[144:145], v[64:65], v[64:65]
	v_pk_mul_f32 v[146:147], v[52:53], v[52:53]
	v_pk_mul_f32 v[148:149], v[60:61], v[60:61]
	v_mov_b32_e32 v67, v66
	v_pk_fma_f32 v[148:149], v[12:13], v[12:13], v[148:149]
	v_pk_fma_f32 v[146:147], v[4:5], v[4:5], v[146:147]
	v_pk_fma_f32 v[144:145], v[16:17], v[16:17], v[144:145]
	v_pk_fma_f32 v[142:143], v[8:9], v[8:9], v[142:143]
	v_pk_fma_f32 v[140:141], v[10:11], v[10:11], v[140:141]
	v_pk_fma_f32 v[138:139], v[2:3], v[2:3], v[138:139]
	v_pk_fma_f32 v[132:133], v[14:15], v[14:15], v[132:133]
	v_pk_fma_f32 v[130:131], v[6:7], v[6:7], v[130:131]
	v_permlane16_swap_b32_e32 v66, v67
	v_pk_add_f32 v[130:131], v[130:131], v[132:133]
	v_pk_add_f32 v[132:133], v[138:139], v[140:141]
	v_pk_add_f32 v[138:139], v[142:143], v[144:145]
	v_pk_add_f32 v[140:141], v[146:147], v[148:149]
	v_mfma_f32_32x32x16_bf16 v[18:33], v[74:77], v[78:81], v[18:33]
	v_add_f32_e32 v136, v66, v67
	ds_read_b128 v[70:73], v134 offset:512
	ds_read_b128 v[66:69], v134 offset:544
	ds_read_b128 v[78:81], v134 offset:576
	ds_read_b128 v[74:77], v134 offset:608
	ds_read_b128 v[82:85], v134 offset:640
	ds_read_b128 v[90:93], v134 offset:672
	ds_read_b128 v[86:89], v134 offset:704
	ds_read_b128 v[94:97], v134 offset:736
	v_pk_add_f32 v[138:139], v[140:141], v[138:139]
	v_pk_add_f32 v[130:131], v[132:133], v[130:131]
	s_waitcnt lgkmcnt(8)
	v_pk_mul_f32 v[140:141], v[126:127], v[62:63]
	v_pk_mov_b32 v[132:133], v[130:131], v[138:139] op_sel:[1,0]
	v_mov_b32_e32 v131, v139
	v_pk_mul_f32 v[138:139], v[122:123], v[54:55]
	v_pk_mul_f32 v[142:143], v[114:115], v[50:51]
	v_pk_mul_f32 v[144:145], v[118:119], v[58:59]
	v_pk_mul_f32 v[146:147], v[124:125], v[56:57]
	v_pk_mul_f32 v[148:149], v[128:129], v[64:65]
	v_pk_mul_f32 v[154:155], v[116:117], v[52:53]
	v_pk_mul_f32 v[156:157], v[120:121], v[60:61]
	v_pk_fma_f32 v[154:155], v[104:105], v[4:5], v[154:155]
	v_pk_fma_f32 v[156:157], v[112:113], v[12:13], v[156:157]
	v_pk_fma_f32 v[148:149], v[108:109], v[16:17], v[148:149]
	v_pk_fma_f32 v[146:147], v[100:101], v[8:9], v[146:147]
	v_pk_fma_f32 v[144:145], v[110:111], v[10:11], v[144:145]
	v_pk_fma_f32 v[142:143], v[102:103], v[2:3], v[142:143]
	v_pk_fma_f32 v[140:141], v[106:107], v[14:15], v[140:141]
	v_pk_fma_f32 v[138:139], v[98:99], v[6:7], v[138:139]
	v_pk_add_f32 v[130:131], v[132:133], v[130:131]
	v_pk_add_f32 v[138:139], v[138:139], v[140:141]
	v_pk_add_f32 v[140:141], v[142:143], v[144:145]
	v_pk_add_f32 v[142:143], v[146:147], v[148:149]
	v_pk_add_f32 v[144:145], v[154:155], v[156:157]
	v_pk_add_f32 v[132:133], v[130:131], v[130:131] op_sel:[0,1] op_sel_hi:[1,0]
	v_pk_add_f32 v[142:143], v[144:145], v[142:143]
	v_pk_add_f32 v[138:139], v[140:141], v[138:139]
	v_add_f32_e32 v133, v142, v143
	v_add_f32_e32 v130, v138, v139
	s_waitcnt lgkmcnt(2)
	v_pk_mul_f32 v[138:139], v[90:91], v[54:55]
	s_waitcnt lgkmcnt(0)
	v_pk_mul_f32 v[140:141], v[94:95], v[62:63]
	v_pk_mul_f32 v[142:143], v[82:83], v[50:51]
	v_pk_mul_f32 v[144:145], v[86:87], v[58:59]
	v_pk_mul_f32 v[146:147], v[92:93], v[56:57]
	v_pk_mul_f32 v[148:149], v[96:97], v[64:65]
	v_pk_mul_f32 v[154:155], v[84:85], v[52:53]
	v_pk_mul_f32 v[156:157], v[88:89], v[60:61]
	v_add_f32_e32 v130, v130, v133
	v_pk_fma_f32 v[156:157], v[80:81], v[12:13], v[156:157]
	v_pk_fma_f32 v[154:155], v[72:73], v[4:5], v[154:155]
	v_pk_fma_f32 v[148:149], v[76:77], v[16:17], v[148:149]
	v_pk_fma_f32 v[146:147], v[68:69], v[8:9], v[146:147]
	v_pk_fma_f32 v[144:145], v[78:79], v[10:11], v[144:145]
	v_pk_fma_f32 v[142:143], v[70:71], v[2:3], v[142:143]
	v_pk_fma_f32 v[140:141], v[74:75], v[14:15], v[140:141]
	v_pk_fma_f32 v[138:139], v[66:67], v[6:7], v[138:139]
	v_mov_b32_e32 v133, v130
	v_pk_add_f32 v[138:139], v[138:139], v[140:141]
	v_pk_add_f32 v[140:141], v[142:143], v[144:145]
	v_pk_add_f32 v[142:143], v[146:147], v[148:149]
	v_pk_add_f32 v[144:145], v[154:155], v[156:157]
	v_permlane32_swap_b32_e32 v130, v133
	v_pk_add_f32 v[142:143], v[144:145], v[142:143]
	v_add_f32_e32 v160, v130, v133
	v_pk_add_f32 v[138:139], v[140:141], v[138:139]
	v_add_f32_e32 v133, v142, v143
	v_pk_add_f32 v[140:141], v[26:27], v[42:43]
	v_pk_add_f32 v[142:143], v[28:29], v[44:45]
	v_pk_add_f32 v[144:145], v[20:21], v[36:37]
	v_pk_add_f32 v[146:147], v[32:33], v[48:49]
	v_pk_add_f32 v[148:149], v[24:25], v[40:41]
	v_pk_add_f32 v[154:155], v[30:31], v[46:47]
	v_pk_add_f32 v[156:157], v[22:23], v[38:39]
	v_pk_add_f32 v[158:159], v[18:19], v[34:35]
	v_pk_add_f32 v[154:155], v[156:157], v[154:155]
	v_pk_add_f32 v[146:147], v[148:149], v[146:147]
	v_pk_add_f32 v[142:143], v[144:145], v[142:143]
	v_pk_add_f32 v[140:141], v[158:159], v[140:141]
	v_pk_add_f32 v[142:143], v[142:143], v[146:147]
	v_pk_add_f32 v[140:141], v[140:141], v[154:155]
	v_add_f32_e32 v130, v138, v139
	v_pk_mov_b32 v[144:145], v[140:141], v[142:143] op_sel:[1,0]
	v_mov_b32_e32 v141, v143
	v_pk_add_f32 v[140:141], v[144:145], v[140:141]
	v_add_f32_e32 v133, v130, v133
	v_pk_add_f32 v[140:141], v[140:141], v[140:141] op_sel:[0,1] op_sel_hi:[1,0]
	v_mov_b32_e32 v131, v132
	v_mov_b32_e32 v130, v140
	s_nop 1
	v_permlane32_swap_b32_e32 v140, v130
	v_add_f32_e32 v130, v140, v130
	v_fmamk_f32 v49, v130, 0xbc800000, v49
	v_fmamk_f32 v48, v130, 0xbc800000, v48
	v_fmamk_f32 v47, v130, 0xbc800000, v47
	v_fmamk_f32 v46, v130, 0xbc800000, v46
	v_fmamk_f32 v45, v130, 0xbc800000, v45
	v_fmamk_f32 v44, v130, 0xbc800000, v44
	v_fmamk_f32 v43, v130, 0xbc800000, v43
	v_fmamk_f32 v42, v130, 0xbc800000, v42
	v_fmamk_f32 v41, v130, 0xbc800000, v41
	v_fmamk_f32 v40, v130, 0xbc800000, v40
	v_fmamk_f32 v39, v130, 0xbc800000, v39
	v_fmamk_f32 v38, v130, 0xbc800000, v38
	v_fmamk_f32 v37, v130, 0xbc800000, v37
	v_fmamk_f32 v36, v130, 0xbc800000, v36
	v_fmamk_f32 v35, v130, 0xbc800000, v35
	v_fmac_f32_e32 v34, 0xbc800000, v130
	v_fmamk_f32 v33, v130, 0xbc800000, v33
	v_fmamk_f32 v32, v130, 0xbc800000, v32
	v_fmamk_f32 v31, v130, 0xbc800000, v31
	v_fmamk_f32 v30, v130, 0xbc800000, v30
	v_fmamk_f32 v29, v130, 0xbc800000, v29
	v_fmamk_f32 v28, v130, 0xbc800000, v28
	v_fmamk_f32 v27, v130, 0xbc800000, v27
	v_fmamk_f32 v26, v130, 0xbc800000, v26
	v_fmamk_f32 v25, v130, 0xbc800000, v25
	v_fmamk_f32 v24, v130, 0xbc800000, v24
	v_fmamk_f32 v23, v130, 0xbc800000, v23
	v_fmamk_f32 v22, v130, 0xbc800000, v22
	v_fmamk_f32 v21, v130, 0xbc800000, v21
	v_fmamk_f32 v20, v130, 0xbc800000, v20
	v_fmamk_f32 v19, v130, 0xbc800000, v19
	v_fmac_f32_e32 v18, 0xbc800000, v130
	v_pk_mul_f32 v[140:141], v[38:39], v[38:39]
	v_pk_mul_f32 v[142:143], v[46:47], v[46:47]
	v_pk_mul_f32 v[144:145], v[34:35], v[34:35]
	v_pk_mul_f32 v[146:147], v[42:43], v[42:43]
	v_pk_mul_f32 v[148:149], v[40:41], v[40:41]
	v_pk_mul_f32 v[154:155], v[48:49], v[48:49]
	v_pk_mul_f32 v[156:157], v[36:37], v[36:37]
	v_pk_mul_f32 v[158:159], v[44:45], v[44:45]
	v_pk_fma_f32 v[156:157], v[20:21], v[20:21], v[156:157]
	v_pk_fma_f32 v[158:159], v[28:29], v[28:29], v[158:159]
	v_pk_fma_f32 v[154:155], v[32:33], v[32:33], v[154:155]
	v_pk_fma_f32 v[148:149], v[24:25], v[24:25], v[148:149]
	v_pk_fma_f32 v[146:147], v[26:27], v[26:27], v[146:147]
	v_pk_fma_f32 v[144:145], v[18:19], v[18:19], v[144:145]
	v_pk_fma_f32 v[142:143], v[30:31], v[30:31], v[142:143]
	v_pk_fma_f32 v[140:141], v[22:23], v[22:23], v[140:141]
	v_permlane32_swap_b32_e32 v132, v131
	v_pk_add_f32 v[140:141], v[140:141], v[142:143]
	v_pk_add_f32 v[142:143], v[144:145], v[146:147]
	v_pk_add_f32 v[144:145], v[148:149], v[154:155]
	v_pk_add_f32 v[146:147], v[156:157], v[158:159]
	v_pk_add_f32 v[140:141], v[142:143], v[140:141]
	v_pk_add_f32 v[144:145], v[146:147], v[144:145]
	v_pk_mul_f32 v[122:123], v[122:123], v[38:39]
	v_pk_mov_b32 v[142:143], v[140:141], v[144:145] op_sel:[1,0]
	v_mov_b32_e32 v141, v145
	v_pk_add_f32 v[140:141], v[142:143], v[140:141]
	v_pk_mul_f32 v[126:127], v[126:127], v[46:47]
	v_pk_add_f32 v[140:141], v[140:141], v[140:141] op_sel:[0,1] op_sel_hi:[1,0]
	v_pk_mul_f32 v[114:115], v[114:115], v[34:35]
	v_mov_b32_e32 v130, v140
	s_nop 1
	v_permlane32_swap_b32_e32 v140, v130
	v_mov_b32_e32 v141, v132
	v_pk_add_f32 v[130:131], v[140:141], v[130:131]
	v_pk_mul_f32 v[118:119], v[118:119], v[42:43]
	v_pk_fma_f32 v[130:131], v[130:131], s[0:1], v[152:153] op_sel_hi:[1,0,0]
	v_pk_mul_f32 v[124:125], v[124:125], v[40:41]
	v_mul_f32_e32 v132, 0x4b800000, v131
	v_cmp_gt_f32_e32 vcc, s1, v131
	v_pk_mul_f32 v[128:129], v[128:129], v[48:49]
	v_pk_mul_f32 v[116:117], v[116:117], v[36:37]
	v_pk_mul_f32 v[120:121], v[120:121], v[44:45]
	v_cndmask_b32_e32 v131, v131, v132, vcc
	v_mul_f32_e32 v132, 0x4b800000, v130
	v_cmp_gt_f32_e64 s[0:1], s1, v130
	v_pk_fma_f32 v[112:113], v[112:113], v[28:29], v[120:121]
	v_pk_fma_f32 v[104:105], v[104:105], v[20:21], v[116:117]
	v_pk_fma_f32 v[108:109], v[108:109], v[32:33], v[128:129]
	v_pk_fma_f32 v[100:101], v[100:101], v[24:25], v[124:125]
	v_pk_fma_f32 v[110:111], v[110:111], v[26:27], v[118:119]
	v_pk_fma_f32 v[102:103], v[102:103], v[18:19], v[114:115]
	v_pk_fma_f32 v[106:107], v[106:107], v[30:31], v[126:127]
	v_pk_fma_f32 v[98:99], v[98:99], v[22:23], v[122:123]
	v_rsq_f32_e32 v131, v131
	v_cndmask_b32_e64 v130, v130, v132, s[0:1]
	v_pk_add_f32 v[98:99], v[98:99], v[106:107]
	v_pk_add_f32 v[102:103], v[102:103], v[110:111]
	v_pk_add_f32 v[100:101], v[100:101], v[108:109]
	v_pk_add_f32 v[104:105], v[104:105], v[112:113]
	v_rsq_f32_e32 v132, v130
	v_pk_add_f32 v[100:101], v[104:105], v[100:101]
	v_pk_add_f32 v[98:99], v[102:103], v[98:99]
	v_mul_f32_e32 v130, 0x45800000, v131
	v_add_f32_e32 v98, v98, v99
	v_add_f32_e32 v99, v100, v101
	v_add_f32_e32 v98, v98, v99
	v_mov_b32_e32 v99, v98
	v_pk_mul_f32 v[90:91], v[90:91], v[38:39]
	v_pk_mul_f32 v[94:95], v[94:95], v[46:47]
	v_pk_mul_f32 v[82:83], v[82:83], v[34:35]
	v_pk_mul_f32 v[86:87], v[86:87], v[42:43]
	v_cndmask_b32_e32 v130, v131, v130, vcc
	v_mul_f32_e32 v131, 0x45800000, v132
	v_permlane32_swap_b32_e32 v98, v99
	v_pk_fma_f32 v[78:79], v[78:79], v[26:27], v[86:87]
	v_pk_fma_f32 v[70:71], v[70:71], v[18:19], v[82:83]
	v_pk_fma_f32 v[74:75], v[74:75], v[30:31], v[94:95]
	v_pk_fma_f32 v[66:67], v[66:67], v[22:23], v[90:91]
	v_cndmask_b32_e64 v131, v132, v131, s[0:1]
	v_add_f32_e32 v98, v98, v99
	v_pk_add_f32 v[66:67], v[66:67], v[74:75]
	v_pk_add_f32 v[70:71], v[70:71], v[78:79]
	v_mul_f32_e32 v139, v160, v130
	v_mul_f32_e32 v98, v98, v131
	v_pk_add_f32 v[66:67], v[70:71], v[66:67]
	v_cmp_gt_u32_e32 vcc, 32, v1
	v_add_f32_e32 v66, v66, v67
	v_pk_mul_f32 v[92:93], v[92:93], v[40:41]
	v_cndmask_b32_e32 v67, v98, v139, vcc
	v_add_f32_e32 v67, s12, v67
	v_pk_mul_f32 v[96:97], v[96:97], v[48:49]
	v_pk_mul_f32 v[84:85], v[84:85], v[36:37]
	v_pk_mul_f32 v[88:89], v[88:89], v[44:45]
	v_mul_f32_e32 v67, 0xbfb8aa3b, v67
	v_pk_fma_f32 v[80:81], v[80:81], v[28:29], v[88:89]
	v_pk_fma_f32 v[72:73], v[72:73], v[20:21], v[84:85]
	v_pk_fma_f32 v[76:77], v[76:77], v[32:33], v[96:97]
	v_pk_fma_f32 v[68:69], v[68:69], v[24:25], v[92:93]
	v_exp_f32_e32 v70, v67
	v_pk_add_f32 v[68:69], v[68:69], v[76:77]
	v_pk_add_f32 v[72:73], v[72:73], v[80:81]
	v_cmp_lt_i32_e64 s[0:1], 0, v151
	v_pk_add_f32 v[68:69], v[72:73], v[68:69]
	v_mov_b32_e32 v137, v136
	v_add_f32_e32 v67, v68, v69
	v_add_f32_e32 v67, v66, v67
	v_add_f32_e32 v66, 1.0, v70
	v_rcp_f32_e32 v66, v66
	v_mov_b32_e32 v69, 0xff800000
	v_mov_b32_e32 v138, v133
	v_mov_b32_e32 v68, v67
	v_cndmask_b32_e64 v70, v69, v66, s[0:1]
	v_mbcnt_lo_u32_b32 v66, -1, 0
	v_mbcnt_hi_u32_b32 v66, -1, v66
	v_permlane32_swap_b32_e32 v136, v137
	v_permlane32_swap_b32_e32 v133, v138
	v_permlane32_swap_b32_e32 v67, v68
	v_and_b32_e32 v86, 64, v66
	s_mov_b32 s14, 8
	s_mov_b32 s13, 0
	v_mov_b32_e32 v66, 0
	s_waitcnt lgkmcnt(0)
